# baseline (speedup 1.0000x reference)
.LBB1_51:
	s_or_b64 exec, exec, s[2:3]
	v_mad_i64_i32 v[22:23], s[2:3], v17, s56, 0
	v_mad_i64_i32 v[18:19], s[2:3], v18, s56, 0
	v_mad_i64_i32 v[24:25], s[2:3], v174, s56, 0
	v_readlane_b32 s3, v230, 8
	s_mov_b64 s[4:5], 0x80
	v_lshl_add_u64 v[6:7], v[6:7], 0, s[4:5]
	v_add_u32_e32 v128, s3, v16
	v_add_u32_e32 v129, 0x2000, v128
	v_readfirstlane_b32 s2, v128
	s_mov_b32 m0, s2
	v_readfirstlane_b32 s2, v129
	v_add_u32_e32 v130, 0x8000, v120
	v_mov_b32_e32 v66, 0
	v_mov_b32_e32 v67, 0
	v_mov_b32_e32 v68, 0
	v_mov_b32_e32 v69, 0
	v_mov_b32_e32 v78, 0
	v_mov_b32_e32 v79, 0
	v_mov_b32_e32 v80, 0
	v_mov_b32_e32 v81, 0
	v_mov_b32_e32 v82, 0
	v_mov_b32_e32 v83, 0
	v_mov_b32_e32 v84, 0
	v_mov_b32_e32 v85, 0
	v_mov_b32_e32 v86, 0
	v_mov_b32_e32 v87, 0
	v_mov_b32_e32 v88, 0
	v_mov_b32_e32 v89, 0
	v_mov_b32_e32 v90, 0
	v_mov_b32_e32 v91, 0
	v_mov_b32_e32 v92, 0
	v_mov_b32_e32 v93, 0
	v_mov_b32_e32 v94, 0
	v_mov_b32_e32 v95, 0
	v_mov_b32_e32 v96, 0
	v_mov_b32_e32 v97, 0
	v_mov_b32_e32 v26, 0
	v_mov_b32_e32 v27, 0
	v_mov_b32_e32 v28, 0
	v_mov_b32_e32 v29, 0
	v_mov_b32_e32 v30, 0
	v_mov_b32_e32 v31, 0
	v_mov_b32_e32 v32, 0
	v_mov_b32_e32 v33, 0
	v_mov_b32_e32 v34, 0
	v_mov_b32_e32 v35, 0
	v_mov_b32_e32 v36, 0
	v_mov_b32_e32 v37, 0
	v_mov_b32_e32 v38, 0
	v_mov_b32_e32 v39, 0
	v_mov_b32_e32 v40, 0
	v_mov_b32_e32 v41, 0
	v_mov_b32_e32 v46, 0
	v_mov_b32_e32 v47, 0
	v_mov_b32_e32 v48, 0
	v_mov_b32_e32 v49, 0
	v_mov_b32_e32 v54, 0
	v_mov_b32_e32 v55, 0
	v_mov_b32_e32 v56, 0
	v_mov_b32_e32 v57, 0
	v_mov_b32_e32 v42, 0
	v_mov_b32_e32 v43, 0
	v_mov_b32_e32 v44, 0
	v_mov_b32_e32 v45, 0
	v_mov_b32_e32 v50, 0
	v_mov_b32_e32 v51, 0
	v_mov_b32_e32 v52, 0
	v_mov_b32_e32 v53, 0
	v_mov_b32_e32 v58, 0
	v_mov_b32_e32 v59, 0
	v_mov_b32_e32 v60, 0
	v_mov_b32_e32 v61, 0
	v_mov_b32_e32 v62, 0
	v_mov_b32_e32 v63, 0
	v_mov_b32_e32 v64, 0
	v_mov_b32_e32 v65, 0
	v_mov_b32_e32 v70, 0
	v_mov_b32_e32 v71, 0
	v_mov_b32_e32 v72, 0
	v_mov_b32_e32 v73, 0
	v_mov_b32_e32 v74, 0
	v_mov_b32_e32 v75, 0
	v_mov_b32_e32 v76, 0
	v_mov_b32_e32 v77, 0
	s_waitcnt vmcnt(4)
	s_barrier
	global_load_lds_dwordx4 v[6:7], off
	v_lshl_add_u64 v[6:7], v[8:9], 0, s[4:5]
	s_mov_b32 m0, s2
	v_readfirstlane_b32 s2, v130
	v_add_u32_e32 v131, 0xa000, v120
	global_load_lds_dwordx4 v[6:7], off
	v_lshl_add_u64 v[6:7], v[10:11], 0, s[4:5]
	s_mov_b32 m0, s2
	v_readfirstlane_b32 s2, v131
	global_load_lds_dwordx4 v[6:7], off
	v_lshl_add_u64 v[6:7], v[12:13], 0, s[4:5]
	s_mov_b32 m0, s2
	s_mov_b64 s[4:5], 0x24080
	global_load_lds_dwordx4 v[6:7], off
	v_lshl_add_u64 v[6:7], v[14:15], 0, s[4:5]
	v_readlane_b32 s4, v230, 9
	v_lshl_add_u64 v[8:9], v[6:7], 0, v[22:23]
	v_lshl_add_u64 v[8:9], v[8:9], 0, v[2:3]
	v_add_u32_e32 v132, s4, v16
	v_add_u32_e32 v133, 0x2000, v132
	v_readfirstlane_b32 s2, v132
	s_mov_b32 m0, s2
	v_lshl_add_u64 v[6:7], v[6:7], 0, v[18:19]
	v_readfirstlane_b32 s2, v133
	global_load_lds_dwordx4 v[8:9], off
	v_lshl_add_u64 v[6:7], v[6:7], 0, v[4:5]
	s_mov_b32 m0, s2
	v_and_b32_e32 v177, 15, v175
	global_load_lds_dwordx4 v[6:7], off
	v_and_b32_e32 v6, 64, v175
	v_lshlrev_b32_e32 v8, 2, v175
	v_cmp_ne_u32_e32 vcc, 0, v6
	v_and_b32_e32 v6, 48, v175
	v_lshlrev_b32_e32 v7, 6, v177
	v_and_b32_e32 v8, 32, v8
	v_bitop3_b32 v7, v7, v8, v6 bitop3:0x36
	v_readlane_b32 s2, v230, 6
	v_ashrrev_i32_e32 v10, 2, v175
	v_and_b32_e32 v180, 0xffffffe0, v10
	v_add_u32_e32 v9, s2, v7
	v_readlane_b32 s2, v230, 7
	v_add_u32_e32 v11, s3, v7
	v_add_u32_e32 v12, s4, v7
	v_add_u32_e32 v10, s2, v7
	v_add_u32_e32 v14, 0, v7
	v_lshlrev_b32_e32 v7, 6, v175
	s_movk_i32 s2, 0x3c0
	v_mul_u32_u24_e32 v20, 0x600, v118
	v_mov_b32_e32 v21, v109
	v_and_or_b32 v6, v7, s2, v6
	v_lshl_add_u64 v[2:3], v[22:23], 0, v[2:3]
	v_xad_u32 v8, v6, v8, 0
	v_lshl_add_u64 v[6:7], v[2:3], 0, v[20:21]
	v_lshl_add_u64 v[4:5], v[18:19], 0, v[4:5]
	v_lshl_add_u64 v[102:103], s[42:43], 0, v[6:7]
	v_lshl_add_u64 v[6:7], v[4:5], 0, v[20:21]
	v_lshl_add_u64 v[104:105], s[42:43], 0, v[6:7]
	v_lshl_add_u64 v[6:7], v[2:3], 0, v[24:25]
	v_lshl_add_u64 v[2:3], v[2:3], 0, v[108:109]
	s_waitcnt vmcnt(6)
	v_cndmask_b32_e64 v179, 0, 48, vcc
	v_lshlrev_b32_e32 v15, 7, v180
	v_lshl_add_u64 v[114:115], s[42:43], 0, v[2:3]
	v_lshl_add_u64 v[2:3], v[4:5], 0, v[108:109]
	v_lshlrev_b32_e32 v13, 7, v179
	v_or_b32_e32 v16, 0x800, v15
	v_lshl_add_u64 v[110:111], s[44:45], 0, v[6:7]
	v_lshl_add_u64 v[6:7], v[4:5], 0, v[24:25]
	v_lshl_add_u64 v[116:117], s[42:43], 0, v[2:3]
	v_mov_b32_e32 v2, 0
	v_lshl_add_u64 v[112:113], s[44:45], 0, v[6:7]
	s_mov_b32 s4, -2
	s_mov_b64 s[2:3], 0
	v_add_u32_e32 v135, v9, v13
	v_add_u32_e32 v121, v14, v15
	v_add_u32_e32 v108, v8, v16
	v_add_u32_e32 v134, v10, v13
	v_add_u32_e32 v127, v11, v13
	v_add_u32_e32 v124, v12, v13
	v_mov_b32_e32 v3, v2
	v_mov_b32_e32 v4, v2
	v_mov_b32_e32 v5, v2
	v_mov_b32_e32 v6, v2
	v_mov_b32_e32 v7, v2
	v_mov_b32_e32 v8, v2
	v_mov_b32_e32 v9, v2
	v_mov_b32_e32 v10, v2
	v_mov_b32_e32 v11, v2
	v_mov_b32_e32 v12, v2
	v_mov_b32_e32 v13, v2
	v_mov_b32_e32 v14, v2
	v_mov_b32_e32 v15, v2
	v_mov_b32_e32 v16, v2
	v_mov_b32_e32 v17, v2
	v_mov_b32_e32 v18, v2
	v_mov_b32_e32 v19, v2
	v_mov_b32_e32 v20, v2
	v_mov_b32_e32 v21, v2
	v_mov_b32_e32 v22, v2
	v_mov_b32_e32 v23, v2
	v_mov_b32_e32 v24, v2
	v_mov_b32_e32 v25, v2
	s_barrier

.LBB1_65:
	s_or_b64 exec, exec, s[2:3]
	v_readlane_b32 s2, v230, 8
	v_mad_i64_i32 v[22:23], s[0:1], v17, s56, 0
	v_mad_i64_i32 v[18:19], s[0:1], v18, s56, 0
	v_mad_i64_i32 v[24:25], s[0:1], v120, s56, 0
	v_add_u32_e32 v137, s2, v16
	s_mov_b64 s[4:5], 0x80
	v_readfirstlane_b32 s0, v137
	v_add_u32_e32 v138, 0x2000, v137
	v_lshl_add_u64 v[6:7], v[6:7], 0, s[4:5]
	s_mov_b32 m0, s0
	v_readfirstlane_b32 s0, v138
	v_add_u32_e32 v139, 0x8000, v129
	v_mov_b32_e32 v46, 0
	v_mov_b32_e32 v47, 0
	v_mov_b32_e32 v48, 0
	v_mov_b32_e32 v49, 0
	v_mov_b32_e32 v74, 0
	v_mov_b32_e32 v75, 0
	v_mov_b32_e32 v76, 0
	v_mov_b32_e32 v77, 0
	v_mov_b32_e32 v86, 0
	v_mov_b32_e32 v87, 0
	v_mov_b32_e32 v88, 0
	v_mov_b32_e32 v89, 0
	v_mov_b32_e32 v90, 0
	v_mov_b32_e32 v91, 0
	v_mov_b32_e32 v92, 0
	v_mov_b32_e32 v93, 0
	v_mov_b32_e32 v94, 0
	v_mov_b32_e32 v95, 0
	v_mov_b32_e32 v96, 0
	v_mov_b32_e32 v97, 0
	v_mov_b32_e32 v26, 0
	v_mov_b32_e32 v27, 0
	v_mov_b32_e32 v28, 0
	v_mov_b32_e32 v29, 0
	v_mov_b32_e32 v34, 0
	v_mov_b32_e32 v35, 0
	v_mov_b32_e32 v36, 0
	v_mov_b32_e32 v37, 0
	v_mov_b32_e32 v50, 0
	v_mov_b32_e32 v51, 0
	v_mov_b32_e32 v52, 0
	v_mov_b32_e32 v53, 0
	v_mov_b32_e32 v30, 0
	v_mov_b32_e32 v31, 0
	v_mov_b32_e32 v32, 0
	v_mov_b32_e32 v33, 0
	v_mov_b32_e32 v38, 0
	v_mov_b32_e32 v39, 0
	v_mov_b32_e32 v40, 0
	v_mov_b32_e32 v41, 0
	v_mov_b32_e32 v54, 0
	v_mov_b32_e32 v55, 0
	v_mov_b32_e32 v56, 0
	v_mov_b32_e32 v57, 0
	v_mov_b32_e32 v62, 0
	v_mov_b32_e32 v63, 0
	v_mov_b32_e32 v64, 0
	v_mov_b32_e32 v65, 0
	v_mov_b32_e32 v42, 0
	v_mov_b32_e32 v43, 0
	v_mov_b32_e32 v44, 0
	v_mov_b32_e32 v45, 0
	v_mov_b32_e32 v58, 0
	v_mov_b32_e32 v59, 0
	v_mov_b32_e32 v60, 0
	v_mov_b32_e32 v61, 0
	v_mov_b32_e32 v66, 0
	v_mov_b32_e32 v67, 0
	v_mov_b32_e32 v68, 0
	v_mov_b32_e32 v69, 0
	v_mov_b32_e32 v70, 0
	v_mov_b32_e32 v71, 0
	v_mov_b32_e32 v72, 0
	v_mov_b32_e32 v73, 0
	v_mov_b32_e32 v78, 0
	v_mov_b32_e32 v79, 0
	v_mov_b32_e32 v80, 0
	v_mov_b32_e32 v81, 0
	v_mov_b32_e32 v82, 0
	v_mov_b32_e32 v83, 0
	v_mov_b32_e32 v84, 0
	v_mov_b32_e32 v85, 0
	s_waitcnt vmcnt(4)
	s_barrier
	global_load_lds_dwordx4 v[6:7], off
	v_lshl_add_u64 v[6:7], v[8:9], 0, s[4:5]
	s_mov_b32 m0, s0
	v_readfirstlane_b32 s0, v139
	v_add_u32_e32 v140, 0xa000, v129
	global_load_lds_dwordx4 v[6:7], off
	v_lshl_add_u64 v[6:7], v[10:11], 0, s[4:5]
	s_mov_b32 m0, s0
	v_readfirstlane_b32 s0, v140
	global_load_lds_dwordx4 v[6:7], off
	v_lshl_add_u64 v[6:7], v[12:13], 0, s[4:5]
	s_mov_b32 m0, s0
	s_mov_b64 s[0:1], 0x24080
	v_readlane_b32 s3, v230, 9
	global_load_lds_dwordx4 v[6:7], off
	v_lshl_add_u64 v[6:7], v[14:15], 0, s[0:1]
	v_add_u32_e32 v141, s3, v16
	v_lshl_add_u64 v[8:9], v[6:7], 0, v[22:23]
	v_readfirstlane_b32 s0, v141
	v_add_u32_e32 v142, 0x2000, v141
	v_lshl_add_u64 v[8:9], v[8:9], 0, v[2:3]
	s_mov_b32 m0, s0
	v_lshl_add_u64 v[6:7], v[6:7], 0, v[18:19]
	v_readfirstlane_b32 s0, v142
	global_load_lds_dwordx4 v[8:9], off
	v_lshl_add_u64 v[6:7], v[6:7], 0, v[4:5]
	s_mov_b32 m0, s0
	v_and_b32_e32 v125, 15, v107
	global_load_lds_dwordx4 v[6:7], off
	v_and_b32_e32 v6, 64, v107
	v_lshlrev_b32_e32 v123, 2, v107
	v_cmp_ne_u32_e64 s[0:1], 0, v6
	v_and_b32_e32 v124, 48, v107
	v_lshlrev_b32_e32 v6, 6, v125
	v_and_b32_e32 v7, 32, v123
	v_cndmask_b32_e64 v126, 0, 48, s[0:1]
	v_bitop3_b32 v6, v6, v7, v124 bitop3:0x36
	v_readlane_b32 s0, v230, 6
	v_ashrrev_i32_e32 v9, 2, v107
	v_and_b32_e32 v127, 0xffffffe0, v9
	v_add_u32_e32 v8, s0, v6
	v_readlane_b32 s0, v230, 7
	v_add_u32_e32 v10, s2, v6
	v_add_u32_e32 v11, s3, v6
	v_add_u32_e32 v9, s0, v6
	v_add_u32_e32 v13, 0, v6
	v_lshlrev_b32_e32 v6, 6, v107
	s_movk_i32 s0, 0x3c0
	v_mul_u32_u24_e32 v20, 0x600, v121
	v_mov_b32_e32 v21, v109
	v_and_or_b32 v6, v6, s0, v124
	v_lshl_add_u64 v[2:3], v[22:23], 0, v[2:3]
	v_xad_u32 v15, v6, v7, 0
	v_lshl_add_u64 v[6:7], v[2:3], 0, v[20:21]
	v_lshl_add_u64 v[4:5], v[18:19], 0, v[4:5]
	v_lshl_add_u64 v[104:105], s[40:41], 0, v[6:7]
	v_lshl_add_u64 v[6:7], v[4:5], 0, v[20:21]
	v_lshl_add_u64 v[110:111], s[40:41], 0, v[6:7]
	v_lshl_add_u64 v[6:7], v[2:3], 0, v[24:25]
	v_lshl_add_u64 v[2:3], v[2:3], 0, v[108:109]
	s_waitcnt vmcnt(6)
	v_lshlrev_b32_e32 v14, 7, v127
	v_lshl_add_u64 v[116:117], s[40:41], 0, v[2:3]
	v_lshl_add_u64 v[2:3], v[4:5], 0, v[108:109]
	v_lshlrev_b32_e32 v12, 7, v126
	v_or_b32_e32 v16, 0x800, v14
	v_lshl_add_u64 v[112:113], s[38:39], 0, v[6:7]
	v_lshl_add_u64 v[6:7], v[4:5], 0, v[24:25]
	v_lshl_add_u64 v[118:119], s[40:41], 0, v[2:3]
	v_mov_b32_e32 v2, 0
	v_lshl_add_u64 v[114:115], s[38:39], 0, v[6:7]
	s_mov_b32 s2, -2
	s_mov_b64 s[0:1], 0
	v_add_u32_e32 v144, v8, v12
	v_add_u32_e32 v130, v13, v14
	v_add_u32_e32 v108, v15, v16
	v_add_u32_e32 v143, v9, v12
	v_add_u32_e32 v136, v10, v12
	v_add_u32_e32 v133, v11, v12
	v_mov_b32_e32 v3, v2
	v_mov_b32_e32 v4, v2
	v_mov_b32_e32 v5, v2
	v_mov_b32_e32 v6, v2
	v_mov_b32_e32 v7, v2
	v_mov_b32_e32 v8, v2
	v_mov_b32_e32 v9, v2
	v_mov_b32_e32 v10, v2
	v_mov_b32_e32 v11, v2
	v_mov_b32_e32 v12, v2
	v_mov_b32_e32 v13, v2
	v_mov_b32_e32 v18, v2
	v_mov_b32_e32 v19, v2
	v_mov_b32_e32 v20, v2
	v_mov_b32_e32 v21, v2
	v_mov_b32_e32 v14, v2
	v_mov_b32_e32 v15, v2
	v_mov_b32_e32 v16, v2
	v_mov_b32_e32 v17, v2
	v_mov_b32_e32 v22, v2
	v_mov_b32_e32 v23, v2
	v_mov_b32_e32 v24, v2
	v_mov_b32_e32 v25, v2
	s_barrier
